# speedup vs baseline: 1.0312x; 1.0118x over previous
.LBB2_53:
	s_lshl_b32 s2, s41, 4
	s_mov_b32 s3, 0
	s_lshl_b32 s8, s41, 8
	s_lshl_b64 s[4:5], s[2:3], 10
	s_waitcnt lgkmcnt(0)
	s_add_u32 s6, s26, s4
	s_addc_u32 s7, s27, s5
	v_lshlrev_b32_e32 v46, 4, v68
	v_mov_b32_e32 v47, 0
	s_movk_i32 s2, 0x2000
	v_lshl_add_u64 v[14:15], s[6:7], 0, v[46:47]
	global_load_dwordx4 v[6:9], v46, s[6:7]
	v_add_co_u32_e32 v48, vcc, s2, v14
	s_movk_i32 s4, 0x1000
	s_nop 0
	v_addc_co_u32_e32 v49, vcc, 0, v15, vcc
	global_load_dwordx4 v[38:41], v[48:49], off offset:-4096
	global_load_dwordx4 v[26:29], v46, s[6:7] offset:1024
	v_add_co_u32_e32 v2, vcc, s4, v14
	s_andn2_b32 s43, s43, 63
	s_nop 0
	v_addc_co_u32_e32 v3, vcc, 0, v15, vcc
	global_load_dwordx4 v[42:45], v[2:3], off offset:1024
	global_load_dwordx4 v[34:37], v46, s[6:7] offset:2048
	global_load_dwordx4 v[30:33], v[2:3], off offset:2048
	global_load_dwordx4 v[22:25], v46, s[6:7] offset:3072
	global_load_dwordx4 v[18:21], v[2:3], off offset:3072
	v_or_b32_e32 v52, s43, v69
	v_ashrrev_i32_e32 v53, 31, v52
	v_lshlrev_b64 v[54:55], 2, v[52:53]
	v_lshl_add_u64 v[50:51], s[36:37], 0, v[54:55]
	global_load_dword v68, v[50:51], off
	global_load_dword v76, v[50:51], off offset:64
	v_lshl_add_u64 v[74:75], s[24:25], 0, v[54:55]
	v_mul_u32_u24_e32 v2, 0x410, v69
	v_and_b32_e32 v53, 48, v0
	global_load_dword v77, v[74:75], off
	global_load_dword v78, v[74:75], off offset:64
	v_add3_u32 v62, s8, v2, v53
	s_barrier
	ds_read_b128 v[2:5], v62
	ds_read_b128 v[10:13], v62 offset:64
	global_load_dwordx4 v[58:61], v[48:49], off
	v_mov_b32_e32 v70, 0x4100
	s_movk_i32 s2, 0x3000
	v_add_co_u32_e32 v66, vcc, s2, v14
	s_movk_i32 s2, 0x840
	s_nop 0
	v_addc_co_u32_e32 v67, vcc, 0, v15, vcc
	s_movk_i32 s5, 0x210
	global_load_dwordx4 v[14:17], v[66:67], off offset:3072
	s_waitcnt vmcnt(13) lgkmcnt(1)
	v_mfma_f32_16x16x32_f16 v[6:9], v[2:5], v[6:9], 0
	s_waitcnt vmcnt(12)
	v_mfma_f32_16x16x32_f16 v[38:41], v[2:5], v[38:41], 0
	s_waitcnt vmcnt(11) lgkmcnt(0)
	v_mfma_f32_16x16x32_f16 v[54:57], v[10:13], v[26:29], v[6:9]
	ds_read_b128 v[26:29], v62 offset:192
	s_nop 2
	ds_read_b128 v[6:9], v62 offset:128
	s_waitcnt vmcnt(10)
	v_mfma_f32_16x16x32_f16 v[38:41], v[10:13], v[42:45], v[38:41]
	global_load_dwordx4 v[42:45], v[48:49], off offset:1024
	global_load_dwordx4 v[62:65], v[48:49], off offset:2048
	s_waitcnt vmcnt(11) lgkmcnt(0)
	v_mfma_f32_16x16x32_f16 v[54:57], v[6:9], v[34:37], v[54:57]
	v_lshl_or_b32 v34, v1, 2, 1
	s_waitcnt vmcnt(10)
	v_mfma_f32_16x16x32_f16 v[36:39], v[6:9], v[30:33], v[38:41]
	v_lshl_add_u32 v30, v52, 1, v70
	global_load_dwordx4 v[70:73], v[48:49], off offset:3072
	v_mad_u32_u24 v35, v1, s2, v30
	v_mad_u32_u24 v52, v34, s5, v30
	global_load_dwordx4 v[30:33], v[66:67], off
	global_load_dword v79, v[50:51], off offset:128
	s_waitcnt vmcnt(12)
	v_mfma_f32_16x16x32_f16 v[54:57], v[26:29], v[22:25], v[54:57]
	s_lshl_b32 s2, s41, 3
	s_lshl_b64 s[2:3], s[2:3], 10
	s_add_u32 s2, s16, s2
	s_waitcnt vmcnt(11)
	v_mfma_f32_16x16x32_f16 v[36:39], v[26:29], v[18:21], v[36:39]
	global_load_dwordx4 v[22:25], v[66:67], off offset:1024
	global_load_dwordx4 v[18:21], v[66:67], off offset:2048
	s_nop 0
	global_load_dword v66, v[50:51], off offset:192
	global_load_dword v67, v[74:75], off offset:128
	s_nop 0
	global_load_dword v74, v[74:75], off offset:192
	s_waitcnt vmcnt(15)
	v_add_f32_e32 v40, v68, v54
	v_add_f32_e32 v41, v68, v55
	v_mul_f32_e32 v50, 0x3fb8aa3b, v40
	v_add_f32_e32 v48, v68, v56
	v_mul_f32_e32 v51, 0x3fb8aa3b, v41
	v_exp_f32_e32 v50, v50
	v_add_f32_e32 v49, v68, v57
	v_mul_f32_e32 v54, 0x3fb8aa3b, v48
	v_exp_f32_e32 v51, v51
	v_mul_f32_e32 v55, 0x3fb8aa3b, v49
	v_exp_f32_e32 v54, v54
	v_exp_f32_e32 v55, v55
	v_add_f32_e32 v50, -1.0, v50
	v_cmp_lt_f32_e32 vcc, 0, v40
	s_waitcnt vmcnt(14)
	v_add_f32_e32 v36, v76, v36
	v_add_f32_e32 v37, v76, v37
	v_cndmask_b32_e32 v40, v50, v40, vcc
	v_add_f32_e32 v50, -1.0, v51
	v_cmp_lt_f32_e32 vcc, 0, v41
	v_add_f32_e32 v51, -1.0, v54
	v_add_f32_e32 v54, -1.0, v55
	v_cndmask_b32_e32 v41, v50, v41, vcc
	v_cmp_lt_f32_e32 vcc, 0, v48
	s_waitcnt vmcnt(13)
	v_sub_f32_e32 v40, v40, v77
	v_sub_f32_e32 v41, v41, v77
	v_cndmask_b32_e32 v48, v51, v48, vcc
	v_cmp_lt_f32_e32 vcc, 0, v49
	v_sub_f32_e32 v48, v48, v77
	v_cvt_f16_f32_e32 v40, v40
	v_cndmask_b32_e32 v49, v54, v49, vcc
	v_cvt_f16_f32_e32 v41, v41
	v_sub_f32_e32 v49, v49, v77
	v_cvt_f16_f32_e32 v48, v48
	v_cvt_f16_f32_e32 v49, v49
	v_mul_f32_e32 v50, 0x3fb8aa3b, v36
	ds_write_b16 v35, v40
	v_exp_f32_e32 v40, v50
	ds_write_b16 v52, v41
	ds_write_b16 v52, v48 offset:528
	ds_write_b16 v52, v49 offset:1056
	v_mul_f32_e32 v41, 0x3fb8aa3b, v37
	v_exp_f32_e32 v41, v41
	v_add_f32_e32 v40, -1.0, v40
	v_cmp_lt_f32_e32 vcc, 0, v36
	v_add_f32_e32 v38, v76, v38
	s_waitcnt vmcnt(11)
	v_mfma_f32_16x16x32_f16 v[48:51], v[2:5], v[58:61], 0
	v_cndmask_b32_e32 v36, v40, v36, vcc
	v_add_f32_e32 v40, -1.0, v41
	v_cmp_lt_f32_e32 vcc, 0, v37
	v_sub_f32_e32 v36, v36, v78
	v_cvt_f16_f32_e32 v36, v36
	v_cndmask_b32_e32 v37, v40, v37, vcc
	v_mul_f32_e32 v40, 0x3fb8aa3b, v38
	v_sub_f32_e32 v37, v37, v78
	v_exp_f32_e32 v40, v40
	v_cvt_f16_f32_e32 v37, v37
	ds_write_b16 v35, v36 offset:32
	ds_write_b16 v52, v37 offset:32
	v_add_f32_e32 v36, -1.0, v40
	s_waitcnt vmcnt(9)
	v_mfma_f32_16x16x32_f16 v[40:43], v[10:13], v[42:45], v[48:51]
	v_cmp_lt_f32_e32 vcc, 0, v38
	v_add_f32_e32 v44, v76, v39
	s_addc_u32 s3, s17, s3
	v_cndmask_b32_e32 v54, v36, v38, vcc
	v_mul_f32_e32 v36, 0x3fb8aa3b, v44
	v_exp_f32_e32 v45, v36
	s_waitcnt vmcnt(8)
	v_mfma_f32_16x16x32_f16 v[36:39], v[6:9], v[62:65], v[40:43]
	v_cmp_lt_f32_e32 vcc, 0, v44
	s_waitcnt vmcnt(7)
	v_mfma_f32_16x16x32_f16 v[36:39], v[26:29], v[70:73], v[36:39]
	v_add_f32_e32 v41, -1.0, v45
	v_sub_f32_e32 v40, v54, v78
	v_cndmask_b32_e32 v41, v41, v44, vcc
	s_waitcnt vmcnt(6)
	v_mfma_f32_16x16x32_f16 v[2:5], v[2:5], v[30:33], 0
	s_waitcnt vmcnt(5)
	s_nop 1
	v_add_f32_e32 v36, v79, v36
	v_mul_f32_e32 v42, 0x3fb8aa3b, v36
	v_exp_f32_e32 v42, v42
	s_waitcnt vmcnt(4)
	v_mfma_f32_16x16x32_f16 v[2:5], v[10:13], v[22:25], v[2:5]
	v_cmp_lt_f32_e32 vcc, 0, v36
	v_cvt_f16_f32_e32 v40, v40
	v_add_f32_e32 v42, -1.0, v42
	v_sub_f32_e32 v41, v41, v78
	v_cndmask_b32_e32 v36, v42, v36, vcc
	v_cvt_f16_f32_e32 v41, v41
	s_waitcnt vmcnt(1)
	v_sub_f32_e32 v36, v36, v67
	v_mfma_f32_16x16x32_f16 v[2:5], v[6:9], v[18:21], v[2:5]
	v_cvt_f16_f32_e32 v36, v36
	v_add_f32_e32 v37, v79, v37
	v_mul_f32_e32 v42, 0x3fb8aa3b, v37
	v_add_f32_e32 v38, v79, v38
	v_exp_f32_e32 v42, v42
	ds_write_b16 v52, v40 offset:560
	ds_write_b16 v52, v41 offset:1088
	ds_write_b16 v35, v36 offset:64
	v_mul_f32_e32 v40, 0x3fb8aa3b, v38
	v_add_f32_e32 v30, v79, v39
	v_exp_f32_e32 v40, v40
	v_mul_f32_e32 v31, 0x3fb8aa3b, v30
	v_mfma_f32_16x16x32_f16 v[2:5], v[26:29], v[14:17], v[2:5]
	v_exp_f32_e32 v31, v31
	v_add_f32_e32 v36, -1.0, v42
	v_cmp_lt_f32_e32 vcc, 0, v37
	v_lshl_add_u64 v[18:19], s[2:3], 0, v[46:47]
	v_add_f32_e32 v11, -1.0, v31
	v_cndmask_b32_e32 v36, v36, v37, vcc
	v_add_f32_e32 v37, -1.0, v40
	v_cmp_lt_f32_e32 vcc, 0, v38
	v_add_f32_e32 v2, v66, v2
	v_sub_f32_e32 v36, v36, v67
	v_cndmask_b32_e32 v37, v37, v38, vcc
	v_cmp_lt_f32_e32 vcc, 0, v30
	v_mul_f32_e32 v7, 0x3fb8aa3b, v2
	v_cvt_f16_f32_e32 v36, v36
	v_sub_f32_e32 v10, v37, v67
	v_cndmask_b32_e32 v6, v11, v30, vcc
	v_exp_f32_e32 v7, v7
	v_cvt_f16_f32_e32 v10, v10
	v_sub_f32_e32 v6, v6, v67
	v_cvt_f16_f32_e32 v6, v6
	v_add_f32_e32 v3, v66, v3
	ds_write_b16 v52, v36 offset:64
	ds_write_b16 v52, v10 offset:592
	ds_write_b16 v52, v6 offset:1120
	v_add_f32_e32 v6, -1.0, v7
	v_mul_f32_e32 v7, 0x3fb8aa3b, v3
	v_exp_f32_e32 v7, v7
	v_cmp_lt_f32_e32 vcc, 0, v2
	v_add_f32_e32 v4, v66, v4
	v_add_f32_e32 v5, v66, v5
	v_cndmask_b32_e32 v2, v6, v2, vcc
	v_add_f32_e32 v6, -1.0, v7
	v_mul_f32_e32 v7, 0x3fb8aa3b, v4
	v_exp_f32_e32 v7, v7
	v_cmp_lt_f32_e32 vcc, 0, v3
	s_waitcnt vmcnt(0)
	v_sub_f32_e32 v2, v2, v74
	v_cvt_f16_f32_e32 v2, v2
	v_cndmask_b32_e32 v3, v6, v3, vcc
	v_add_f32_e32 v6, -1.0, v7
	v_mul_f32_e32 v7, 0x3fb8aa3b, v5
	v_exp_f32_e32 v7, v7
	v_cmp_lt_f32_e32 vcc, 0, v4
	v_sub_f32_e32 v3, v3, v74
	v_cvt_f16_f32_e32 v3, v3
	v_cndmask_b32_e32 v4, v6, v4, vcc
	v_add_f32_e32 v6, -1.0, v7
	v_cmp_lt_f32_e32 vcc, 0, v5
	v_sub_f32_e32 v4, v4, v74
	v_cvt_f16_f32_e32 v4, v4
	v_cndmask_b32_e32 v5, v6, v5, vcc
	v_sub_f32_e32 v5, v5, v74
	v_cvt_f16_f32_e32 v5, v5
	ds_write_b16 v35, v2 offset:96
	ds_write_b16 v52, v3 offset:96
	ds_write_b16 v52, v4 offset:624
	ds_write_b16 v52, v5 offset:1152
	s_waitcnt lgkmcnt(0)
	global_load_dwordx4 v[2:5], v46, s[2:3]
	global_load_dwordx4 v[6:9], v46, s[2:3] offset:1024
	global_load_dwordx4 v[10:13], v46, s[2:3] offset:2048
	global_load_dwordx4 v[14:17], v46, s[2:3] offset:3072
	v_add_co_u32_e32 v36, vcc, s4, v18
	v_mad_u32_u24 v35, v69, s5, v53
	s_nop 0
	v_addc_co_u32_e32 v37, vcc, 0, v19, vcc
	global_load_dwordx4 v[18:21], v[36:37], off
	global_load_dwordx4 v[22:25], v[36:37], off offset:1024
	global_load_dwordx4 v[26:29], v[36:37], off offset:2048
	global_load_dwordx4 v[30:33], v[36:37], off offset:3072
	s_barrier
	ds_read_b128 v[36:39], v35 offset:16640
	ds_read_b128 v[40:43], v35 offset:16704
	s_movk_i32 s2, 0x440
	s_waitcnt vmcnt(7) lgkmcnt(1)
	v_mfma_f32_16x16x32_f16 v[2:5], v[36:39], v[2:5], 0
	ds_read_b128 v[36:39], v35 offset:16768
	s_waitcnt vmcnt(6) lgkmcnt(1)
	v_mfma_f32_16x16x32_f16 v[2:5], v[40:43], v[6:9], v[2:5]
	ds_read_b128 v[6:9], v35 offset:16832
	s_waitcnt vmcnt(5) lgkmcnt(1)
	v_mfma_f32_16x16x32_f16 v[2:5], v[36:39], v[10:13], v[2:5]
	ds_read_b128 v[10:13], v35 offset:16896
	s_waitcnt vmcnt(4) lgkmcnt(1)
	v_mfma_f32_16x16x32_f16 v[2:5], v[6:9], v[14:17], v[2:5]
	ds_read_b128 v[6:9], v35 offset:16960
	s_waitcnt vmcnt(3) lgkmcnt(1)
	v_mfma_f32_16x16x32_f16 v[2:5], v[10:13], v[18:21], v[2:5]
	ds_read_b128 v[10:13], v35 offset:17024
	s_waitcnt vmcnt(2) lgkmcnt(1)
	v_mfma_f32_16x16x32_f16 v[2:5], v[6:9], v[22:25], v[2:5]
	ds_read_b128 v[6:9], v35 offset:17088
	s_waitcnt vmcnt(1) lgkmcnt(1)
	v_mfma_f32_16x16x32_f16 v[2:5], v[10:13], v[26:29], v[2:5]
	s_waitcnt vmcnt(0) lgkmcnt(0)
	v_mfma_f32_16x16x32_f16 v[2:5], v[6:9], v[30:33], v[2:5]
	v_lshlrev_b32_e32 v6, 2, v69
	v_lshl_or_b32 v7, s41, 6, v6
	v_mad_u32_u24 v1, v1, s2, v7
	s_movk_i32 s2, 0x110
	s_nop 3
	ds_write_b32 v1, v2
	v_mad_u32_u24 v1, v34, s2, v7
	v_lshlrev_b32_e32 v2, 4, v69
	ds_write2_b32 v1, v3, v4 offset1:68
	ds_write_b32 v1, v5 offset:544
	s_waitcnt lgkmcnt(0)
	global_load_dwordx4 v[8:11], v2, s[24:25] offset:1024
	global_load_dwordx4 v[12:15], v2, s[18:19]
	global_load_dwordx4 v[16:19], v2, s[14:15]
	v_lshrrev_b32_e32 v1, 4, v0
	v_mad_u32_u24 v2, v1, s2, v2
	s_barrier
	ds_read_b128 v[2:5], v2
	s_movk_i32 s2, 0x100
	s_waitcnt vmcnt(2) lgkmcnt(0)
	v_add_f32_e32 v9, v3, v9
	v_add_f32_e32 v8, v2, v8
	s_waitcnt vmcnt(1)
	v_mul_f32_e32 v13, v13, v9
	s_waitcnt vmcnt(0)
	v_mul_f32_e32 v9, v17, v9
	v_add_f32_e32 v10, v4, v10
	v_fmac_f32_e32 v13, v12, v8
	v_fmac_f32_e32 v9, v16, v8
	v_add_f32_e32 v11, v5, v11
	v_fmac_f32_e32 v13, v14, v10
	v_fmac_f32_e32 v9, v18, v10
	v_fmac_f32_e32 v13, v15, v11
	v_fmac_f32_e32 v9, v19, v11
	s_nop 1
	v_add_f32_dpp v13, v13, v13 row_mirror row_mask:0xf bank_mask:0xf
	v_add_f32_dpp v9, v9, v9 row_mirror row_mask:0xf bank_mask:0xf
	s_nop 0
	v_add_f32_dpp v13, v13, v13 row_half_mirror row_mask:0xf bank_mask:0xf
	v_add_f32_dpp v9, v9, v9 row_half_mirror row_mask:0xf bank_mask:0xf
	s_nop 0
	v_add_f32_dpp v13, v13, v13 quad_perm:[2,3,0,1] row_mask:0xf bank_mask:0xf
	v_add_f32_dpp v9, v9, v9 quad_perm:[2,3,0,1] row_mask:0xf bank_mask:0xf
	s_nop 0
	v_add_f32_dpp v7, v13, v13 quad_perm:[1,0,3,2] row_mask:0xf bank_mask:0xf
	v_add_f32_dpp v12, v9, v9 quad_perm:[1,0,3,2] row_mask:0xf bank_mask:0xf
	v_cmp_gt_u32_e32 vcc, s2, v0
	s_and_saveexec_b64 s[2:3], vcc
	s_cbranch_execz .LBB2_57
	v_lshlrev_b32_e32 v0, 2, v1
	ds_read_b32 v0, v0 offset:25152
	s_load_dwordx2 s[2:3], s[0:1], 0x50
	v_cmp_eq_u32_e32 vcc, 0, v69
	s_waitcnt lgkmcnt(0)
	v_add_u32_e32 v0, s33, v0
	v_ashrrev_i32_e32 v1, 31, v0
	s_and_saveexec_b64 s[4:5], vcc
	s_cbranch_execz .LBB2_56
	s_load_dwordx4 s[8:11], s[0:1], 0x58
	v_lshlrev_b64 v[8:9], 2, v[0:1]
	s_waitcnt lgkmcnt(0)
	v_lshl_add_u64 v[10:11], s[10:11], 0, v[8:9]
	v_lshl_add_u64 v[8:9], s[8:9], 0, v[8:9]
	global_store_dword v[8:9], v7, off
	global_store_dword v[10:11], v12, off

.LBB2_57:
	s_endpgm
	s_nop 0
	s_nop 0
	s_nop 0
	s_nop 0
	s_nop 0
	s_nop 0
	s_nop 0
	s_nop 0
	s_nop 0
	s_endpgm
